# gMLP spatial: keep Ws tile, b_s and LN gain/bias of a workgroup's constant channel group across units instead of refetching them (and draining the T stores) every unit
# baseline (speedup 1.0000x reference)
; #define LAS __attribute__((address_space(3)))
; #define INP(k) inp_ptr(k)
; #define SP_LANE() const int tid = opaque_tid(wave), lane = tid & 63, r32 = lane & 31, hi = lane >> 5, c8 = tid & 31, q0 = tid >> 5
; #define SP_LOAD(uu) do { const int ch_ = ch0 + ((uu) >> 3), g_ = (uu) & 7; _Pragma("unroll") for (int i = 0; i < 8; ++i) zin[i] = *(const u32x4*)(Z + (size_t)(ch_ * 128 + q0 + 16 * i) * 4096 + 2048 + 256 * g_ + 8 * c8); \
;         _Pragma("unroll") for (int i = 0; i < 4; ++i) pin[i] = *(const f32x4*)(PART + ((size_t)(ch_ * 128 + (tid >> 2)) * 32 + 8 * (tid & 3)) * 2 + 4 * i); } while (0)
; __device__ __forceinline__ void gmlp_spatial_fused(Frame& F, int j, int row0) {
;     const bf16_t* Z = (const bf16_t*)(F.ws + WS_R1 + R1_Z); const float* PART = (const float*)(F.ws + WS_PART); bf16_t* T = (bf16_t*)(F.ws + WS_R1 + R1_T);
;     LAS f32x2* stl = (LAS f32x2*)(F.lds + MISC_OFF + 1024);
;     LAS float* bsl = (LAS float*)(F.lds + MISC_OFF + 2048);
;     const bf16_t* WSb = (const bf16_t*)(F.ws + WS_WS) + (size_t)j * 8 * 128 * 128; const float* bs = INP(IN_GBS) + j * 8 * 128;
;     const float* lng = INP(IN_GLNG) + j * 2048; const float* lnb = INP(IN_GLNB) + j * 2048;
;     const int wave = F.wave;
;     char* lds = F.ldsg; bf16_t* outl = (bf16_t*)lds; char* wl = lds + 65536;
;     const int nunit = ((TALL - row0) / 128) * 8, ch0 = row0 / 128;
;     ...
;     const unsigned wlds = (unsigned)__builtin_amdgcn_readfirstlane((int)((unsigned)(uintptr_t)wl + (unsigned)wave * 4096u));
;     const int ehalf = wave >> 2, d0 = wave & 3;
;     u32x4 zin[8]; f32x4 pin[4];
;     int u = F.bid;
;     ...
;     if (u < nunit) { SP_LANE(); SP_LOAD(u); }
.LBB0_580:
	s_or_b64 exec, exec, s[2:3]
	s_mov_b32 s28, s53
	s_waitcnt lgkmcnt(0)
	s_barrier
	s_mov_b32 s100, -1
	s_mov_b32 s10, s73
	s_mov_b32 s11, s90
	s_lshl_b32 s29, s28, 12
	v_mbcnt_lo_u32_b32 v0, -1, 0
	v_mbcnt_hi_u32_b32 v0, -1, v0
	s_mov_b64 s[8:9], s[88:89]
	s_mov_b64 s[2:3], s[88:89]
	s_mov_b64 s[0:1], s[88:89]
	s_cmp_ge_i32 s10, s74
	s_cbranch_scc1 .LBB0_589
	s_lshl_b32 s16, s28, 6
	s_add_u32 s4, s94, 0x55800000
	s_addc_u32 s5, s95, 0
	s_add_u32 s6, s94, 0x9d400000
	s_addc_u32 s7, s95, 0
	s_add_u32 s17, s94, 0x87000000
	s_addc_u32 s20, s95, 0
	s_and_b64 s[22:23], s[76:77], exec
	s_cselect_b32 s12, 0x40000, 0
	s_add_u32 s12, s94, s12
	s_addc_u32 s13, s95, 0
	s_load_dwordx2 s[8:9], s[8:9], 0x60
	s_add_u32 s21, s12, 0x3000000
	s_addc_u32 s22, s13, 0
	s_and_b64 s[24:25], s[76:77], exec
	s_cselect_b32 s12, 0x1000, 0
	s_load_dwordx2 s[2:3], s[2:3], 0x48
	s_waitcnt lgkmcnt(0)
	s_add_u32 s78, s8, s12
	s_addc_u32 s79, s9, 0
	s_load_dwordx2 s[0:1], s[0:1], 0x50
	s_and_b64 s[8:9], s[76:77], exec
	s_cselect_b32 s12, 0x2000, 0
	s_add_u32 s8, s2, s12
	s_addc_u32 s9, s3, 0
	s_waitcnt lgkmcnt(0)
	s_add_u32 s23, s0, s12
	s_addc_u32 s24, s1, 0
	s_lshr_b32 s25, s39, 7
	s_add_i32 s26, 0, 0x10000
	s_cmp_lg_u32 s26, -1
	s_cselect_b32 s0, s26, 0
	s_add_i32 s27, s29, s0
	s_lshr_b32 s0, s10, 3
	s_waitcnt vmcnt(5)
	v_mbcnt_lo_u32_b32 v6, -1, 0
	v_mbcnt_hi_u32_b32 v6, -1, v6
	s_add_i32 s0, s0, s25
	v_add_u32_e32 v7, s16, v6
	v_ashrrev_i32_e32 v0, 5, v7
	s_lshl_b32 s0, s0, 7
	v_add_u32_e32 v2, s0, v0
	v_ashrrev_i32_e32 v3, 31, v2
	v_lshlrev_b64 v[2:3], 13, v[2:3]
	s_lshl_b32 s1, s10, 9
	v_lshl_add_u64 v[2:3], s[4:5], 0, v[2:3]
	s_and_b32 s18, s1, 0xe00
	v_lshlrev_b32_e32 v0, 4, v6
	v_and_b32_e32 v0, 0x1f0, v0
	v_lshl_add_u64 v[2:3], v[2:3], 0, s[18:19]
	v_lshl_add_u64 v[2:3], v[2:3], 0, v[0:1]
	v_add_co_u32_e32 v4, vcc, s58, v2
	v_ashrrev_i32_e32 v0, 2, v7
	s_nop 0
	v_addc_co_u32_e32 v5, vcc, 0, v3, vcc
	global_load_dwordx4 v[66:69], v[4:5], off
	v_add_co_u32_e32 v4, vcc, s59, v2
	s_lshl_b32 s1, s28, 9
	s_nop 0
	v_addc_co_u32_e32 v5, vcc, 0, v3, vcc
	global_load_dwordx4 v[70:73], v[4:5], off
	v_add_co_u32_e32 v4, vcc, s60, v2
	s_and_b32 s1, s1, 0x600
	s_nop 0
	v_addc_co_u32_e32 v5, vcc, 0, v3, vcc
	global_load_dwordx4 v[74:77], v[4:5], off
	v_add_co_u32_e32 v4, vcc, s61, v2
	s_lshl_b32 s38, s28, 5
	s_nop 0
	v_addc_co_u32_e32 v5, vcc, 0, v3, vcc
	global_load_dwordx4 v[78:81], v[4:5], off
	v_add_co_u32_e32 v4, vcc, s64, v2
	s_add_i32 s39, s27, 0x400
	s_nop 0
	v_addc_co_u32_e32 v5, vcc, 0, v3, vcc
	global_load_dwordx4 v[82:85], v[4:5], off
	v_add_co_u32_e32 v4, vcc, s65, v2
	s_add_i32 s41, s27, 0x800
	s_nop 0
	v_addc_co_u32_e32 v5, vcc, 0, v3, vcc
	global_load_dwordx4 v[86:89], v[4:5], off
	v_add_co_u32_e32 v4, vcc, s66, v2
	s_add_i32 s48, s27, 0xc00
	s_nop 0
	v_addc_co_u32_e32 v5, vcc, 0, v3, vcc
	v_add_co_u32_e32 v2, vcc, s67, v2
	global_load_dwordx4 v[90:93], v[4:5], off
	s_nop 0
	v_addc_co_u32_e32 v3, vcc, 0, v3, vcc
	global_load_dwordx4 v[94:97], v[2:3], off
	v_add_u32_e32 v2, s0, v0
	v_ashrrev_i32_e32 v3, 31, v2
	v_lshlrev_b64 v[2:3], 8, v[2:3]
	v_lshlrev_b32_e32 v0, 6, v6
	v_lshl_add_u64 v[2:3], s[6:7], 0, v[2:3]
	v_and_b32_e32 v0, 0xc0, v0
	v_lshl_add_u64 v[2:3], v[2:3], 0, v[0:1]
	global_load_dwordx4 v[98:101], v[2:3], off offset:48
	global_load_dwordx4 v[102:105], v[2:3], off offset:32
	global_load_dwordx4 v[106:109], v[2:3], off offset:16
	global_load_dwordx4 v[110:113], v[2:3], off
	s_and_b32 s0, s29, 0xffffc000
	s_lshl_b32 s29, s28, 4
	s_cmp_lg_u32 0, -1
	s_cselect_b32 s2, 0, 0
	s_add_i32 s49, s0, s2
	s_add_i32 s0, s10, s11
	s_add_i32 s49, s49, s1
	s_lshl_b32 s51, s0, 8
	s_lshl_b32 s52, s11, 8
	s_branch .LBB0_583

; __device__ __forceinline__ int v_st(int k, int c) { const int kk = (k & ~0xC) | ((k & 4) << 1) | ((k & 8) >> 1); return ((kk >> 3) * 4 + (c >> 5)) * 512 + ((kk & 7) * 32 + (c & 31)) * 2; }
; __device__ __forceinline__ int v_rd_base(int lane) { return ((lane & 3) << 3) | (((lane >> 2) & 3) << 6) | (((lane >> 4) & 1) << 5) | (((lane >> 5) & 1) << 8); }
; #define SP_LANE() const int tid = opaque_tid(wave), lane = tid & 63, r32 = lane & 31, hi = lane >> 5, c8 = tid & 31, q0 = tid >> 5
; __device__ __forceinline__ void gmlp_spatial_fused(Frame& F, int j, int row0) {
;     ...
;     for (; u < nunit; u += F.G) {
;         const int chunk = ch0 + (u >> 3), g = u & 7;
;         SP_LANE();
;         const int vb = (int)(uintptr_t)lds + ehalf * 16384 + d0 * 512 + att::v_rd_base(lane);
;         unsigned woff[4];
; #pragma unroll
;         for (int i = 0; i < 4; ++i) { const int row = 4 * (4 * wave + i) + (lane >> 4), cpos = (lane & 15) << 4; woff[i] = (unsigned)(row * 256 + (cpos ^ ((row & 7) << 4))); }
;         int sto[8];
; #pragma unroll
;         for (int i = 0; i < 8; ++i) { const int q = q0 + 16 * i, e = 8 * c8; sto[i] = ((q >> 6) * 2 + (e >> 7)) * 16384 + att::v_st(q & 63, e & 127); }
;         if (tid < 128) bsl[tid] = bs[g * 128 + tid];
.LBB0_583:
	s_waitcnt vmcnt(14)
	v_mbcnt_lo_u32_b32 v18, -1, 0
	v_mbcnt_hi_u32_b32 v18, -1, v18
	s_and_b32 s18, s10, 7
	v_add_u32_e32 v19, s16, v18
	s_cmp_eq_u32 s100, s18
	s_cbranch_scc1 .Lsp_skip_bs
	v_cmp_gt_i32_e32 vcc, s56, v19
	s_and_saveexec_b64 s[0:1], vcc
	s_cbranch_execz .LBB0_585
	v_lshl_add_u32 v2, s18, 7, v19
	v_ashrrev_i32_e32 v3, 31, v2
	v_lshl_add_u64 v[2:3], v[2:3], 2, s[78:79]
	global_load_dword v0, v[2:3], off
	v_lshl_add_u32 v2, v19, 2, 0
	v_add_u32_e32 v2, 0x20800, v2
	s_waitcnt vmcnt(0)
	ds_write_b32 v2, v0

; template <int M> __device__ __forceinline__ float swz_xor_f(float v) { return __builtin_bit_cast(float, __builtin_amdgcn_ds_swizzle(__builtin_bit_cast(int, v), (M << 10) | 0x1f)); }
; __device__ __forceinline__ int v_st(int k, int c) { const int kk = (k & ~0xC) | ((k & 4) << 1) | ((k & 8) >> 1); return ((kk >> 3) * 4 + (c >> 5)) * 512 + ((kk & 7) * 32 + (c & 31)) * 2; }
; __device__ __forceinline__ int v_rd_base(int lane) { return ((lane & 3) << 3) | (((lane >> 2) & 3) << 6) | (((lane >> 4) & 1) << 5) | (((lane >> 5) & 1) << 8); }
; __device__ __forceinline__ void gmlp_spatial_fused(Frame& F, int j, int row0) {
;     ...
;         const int vb = (int)(uintptr_t)lds + ehalf * 16384 + d0 * 512 + att::v_rd_base(lane);
;         unsigned woff[4];
; #pragma unroll
;         for (int i = 0; i < 4; ++i) { const int row = 4 * (4 * wave + i) + (lane >> 4), cpos = (lane & 15) << 4; woff[i] = (unsigned)(row * 256 + (cpos ^ ((row & 7) << 4))); }
;         int sto[8];
; #pragma unroll
;         for (int i = 0; i < 8; ++i) { const int q = q0 + 16 * i, e = 8 * c8; sto[i] = ((q >> 6) * 2 + (e >> 7)) * 16384 + att::v_st(q & 63, e & 127); }
;         if (tid < 128) bsl[tid] = bs[g * 128 + tid];
;         { const char* wg = (const char*)(WSb + (size_t)g * 128 * 128);
; #pragma unroll
;           for (int i = 0; i < 4; ++i) pg8::glds16_s(wg, woff[i], wlds + (unsigned)i * 1024u); }
;         { float sm = (pin[0][0] + pin[0][2]) + (pin[1][0] + pin[1][2]) + (pin[2][0] + pin[2][2]) + (pin[3][0] + pin[3][2]), sq = (pin[0][1] + pin[0][3]) + (pin[1][1] + pin[1][3]) + (pin[2][1] + pin[2][3]) + (pin[3][1] + pin[3][3]);
;           sm += swz_xor_f<1>(sm); sq += swz_xor_f<1>(sq); sm += swz_xor_f<2>(sm); sq += swz_xor_f<2>(sq);
;           const float mean = sm * (1.0f / 2048.0f), var = __builtin_fmaxf(sq * (1.0f / 2048.0f) - mean * mean, 0.f);
;           if ((tid & 3) == 0) stl[tid >> 2] = (f32x2){mean, 1.0f / sqrtf(var + LN_EPS)}; }
;         asm volatile("s_waitcnt lgkmcnt(0)" ::: "memory");
;     ...
;         { const f32x4 ga = *(const f32x4*)(lng + 256 * g + 8 * c8), gb = *(const f32x4*)(lng + 256 * g + 8 * c8 + 4), ba = *(const f32x4*)(lnb + 256 * g + 8 * c8), bb = *(const f32x4*)(lnb + 256 * g + 8 * c8 + 4);
.Lsp_skip_bs:
	v_bfe_u32 v0, v18, 4, 2
	v_or_b32_e32 v0, s29, v0
	v_lshlrev_b32_e32 v149, 4, v18
	v_and_b32_e32 v2, 0xf0, v149
	v_lshlrev_b32_e32 v3, 8, v0
	v_and_b32_e32 v4, 48, v18
	v_bitop3_b32 v3, v3, v2, v4 bitop3:0xf6
	v_or_b32_e32 v4, 4, v0
	s_lshl_b32 s0, s18, 15
	v_lshlrev_b32_e32 v5, 8, v4
	v_lshlrev_b32_e32 v4, 4, v4
	v_or_b32_e32 v0, 12, v0
	s_add_u32 s0, s21, s0
	v_and_b32_e32 v4, 0x70, v4
	v_lshlrev_b32_e32 v6, 8, v0
	v_lshlrev_b32_e32 v0, 4, v0
	s_addc_u32 s1, s22, 0
	v_bitop3_b32 v4, v4, v5, v2 bitop3:0xde
	v_or_b32_e32 v5, 0x800, v3
	v_and_b32_e32 v0, 0x70, v0
	v_bitop3_b32 v0, v0, v6, v2 bitop3:0xde
	s_cmp_eq_u32 s100, s18
	s_cbranch_scc1 .Lsp_skip_dma
	s_mov_b32 m0, s27
	s_nop 0
	global_load_lds_dwordx4 v3, s[0:1]
	s_mov_b32 m0, s39
	s_nop 0
	global_load_lds_dwordx4 v4, s[0:1]
	s_mov_b32 m0, s41
	s_nop 0
	global_load_lds_dwordx4 v5, s[0:1]
	s_mov_b32 m0, s48
	s_nop 0
	global_load_lds_dwordx4 v0, s[0:1]
	s_waitcnt vmcnt(4)
.Lsp_skip_dma:
	v_pk_add_f32 v[2:3], v[110:111], v[112:113]
	v_pk_add_f32 v[4:5], v[106:107], v[108:109]
	v_and_b32_e32 v20, 3, v18
	v_pk_add_f32 v[2:3], v[2:3], v[4:5]
	v_pk_add_f32 v[4:5], v[102:103], v[104:105]
	v_cmp_eq_u32_e32 vcc, 0, v20
	v_pk_add_f32 v[2:3], v[2:3], v[4:5]
	v_pk_add_f32 v[4:5], v[98:99], v[100:101]
	s_nop 0
	v_pk_add_f32 v[2:3], v[2:3], v[4:5]
	ds_swizzle_b32 v4, v2 offset:swizzle(SWAP,1)
	ds_swizzle_b32 v5, v3 offset:swizzle(SWAP,1)
	s_waitcnt lgkmcnt(0)
	v_pk_add_f32 v[2:3], v[2:3], v[4:5]
	ds_swizzle_b32 v4, v2 offset:swizzle(SWAP,2)
	ds_swizzle_b32 v5, v3 offset:swizzle(SWAP,2)
	s_and_saveexec_b64 s[0:1], vcc
	s_cbranch_execz .LBB0_587
	s_waitcnt lgkmcnt(0)
	v_pk_add_f32 v[2:3], v[2:3], v[4:5]
	s_mov_b32 s2, 0x3a000000
	v_pk_mul_f32 v[2:3], v[2:3], s[2:3] op_sel_hi:[1,0]
	s_nop 0
	v_fma_f32 v0, -v2, v2, v3
	v_max_f32_e32 v0, 0, v0
	v_add_f32_e32 v0, 0x3727c5ac, v0
	v_mul_f32_e32 v3, 0x4f800000, v0
	v_cmp_gt_f32_e32 vcc, s71, v0
	s_nop 1
	v_cndmask_b32_e32 v0, v0, v3, vcc
	v_sqrt_f32_e32 v3, v0
	s_nop 0
	v_add_u32_e32 v4, -1, v3
	v_fma_f32 v6, -v4, v3, v0
	v_add_u32_e32 v5, 1, v3
	v_cmp_ge_f32_e64 s[2:3], 0, v6
	s_nop 1
	v_cndmask_b32_e64 v4, v3, v4, s[2:3]
	v_fma_f32 v3, -v5, v3, v0
	v_cmp_lt_f32_e64 s[2:3], 0, v3
	s_nop 1
	v_cndmask_b32_e64 v3, v4, v5, s[2:3]
	v_mul_f32_e32 v4, 0x37800000, v3
	v_cndmask_b32_e32 v3, v3, v4, vcc
	v_cmp_class_f32_e32 vcc, v0, v189
	s_nop 1
	v_cndmask_b32_e32 v0, v3, v0, vcc
	v_div_scale_f32 v3, s[2:3], v0, v0, 1.0
	v_rcp_f32_e32 v4, v3
	s_nop 0
	v_fma_f32 v5, -v3, v4, 1.0
	v_fmac_f32_e32 v4, v5, v4
	v_div_scale_f32 v5, vcc, 1.0, v0, 1.0
	v_mul_f32_e32 v6, v5, v4
	v_fma_f32 v7, -v3, v6, v5
	v_fmac_f32_e32 v6, v7, v4
	v_fma_f32 v3, -v3, v6, v5
	v_div_fmas_f32 v3, v3, v4, v6
	v_div_fixup_f32 v3, v3, v0, 1.0
	v_lshl_add_u32 v0, v19, 1, 0
	v_add_u32_e32 v0, 0x20400, v0
	ds_write_b64 v0, v[2:3]
.LBB0_587:
	s_or_b64 exec, exec, s[0:1]
	s_ashr_i32 s0, s10, 3
	s_add_i32 s76, s0, s25
	s_lshl_b32 s0, s18, 8
	s_lshl_b32 s1, s18, 10
	v_and_b32_e32 v147, 31, v18
	s_add_u32 s2, s8, s1
	s_addc_u32 s3, s9, 0
	v_lshlrev_b32_e32 v0, 5, v147
	s_waitcnt lgkmcnt(0)
	s_waitcnt lgkmcnt(0)
	s_barrier
	s_cmp_eq_u32 s100, s18
	s_cbranch_scc1 .Lsp_skip_ln
	global_load_dwordx4 v[2:5], v0, s[2:3] offset:16
	global_load_dwordx4 v[10:13], v0, s[2:3]
	s_add_u32 s2, s23, s1
	s_addc_u32 s3, s24, 0
	global_load_dwordx4 v[6:9], v0, s[2:3] offset:16
	global_load_dwordx4 v[14:17], v0, s[2:3]
	s_branch .Lsp_ln_done
.Lsp_skip_ln:
	s_add_u32 s2, s23, s1
	s_addc_u32 s3, s24, 0
.Lsp_ln_done:
	v_ashrrev_i32_e32 v162, 5, v19
	v_lshlrev_b32_e32 v0, 4, v147
	v_lshrrev_b32_e32 v23, 1, v162
	v_and_b32_e32 v25, 3, v162
	v_and_or_b32 v23, v23, 4, v25
	v_and_b32_e32 v25, 48, v0
	v_bfe_u32 v21, v18, 4, 1
	v_lshlrev_b32_e32 v22, 1, v162
	v_lshl_or_b32 v32, v23, 6, v25
	v_lshrrev_b32_e32 v23, 10, v19
	v_and_b32_e32 v22, 8, v22
	v_and_or_b32 v23, v23, s45, v21
	v_lshlrev_b32_e32 v33, 14, v23
	v_and_or_b32 v23, v162, 48, v22
	v_bfe_u32 v24, v18, 2, 2
	v_lshrrev_b32_e32 v23, 1, v23
	v_add_u32_e32 v160, 16, v162
	v_or_b32_e32 v34, v23, v24
	v_lshrrev_b32_e32 v23, 5, v160
	v_and_or_b32 v23, v23, s45, v21
	v_lshlrev_b32_e32 v35, 14, v23
	v_and_or_b32 v23, v160, 48, v22
	v_lshrrev_b32_e32 v23, 1, v23
	v_add_u32_e32 v158, 32, v162
	v_or_b32_e32 v36, v23, v24
	v_lshrrev_b32_e32 v23, 5, v158
	v_and_or_b32 v23, v23, s45, v21
	v_lshlrev_b32_e32 v37, 14, v23
	v_and_or_b32 v23, v158, 48, v22
	v_lshrrev_b32_e32 v23, 1, v23
	v_add_u32_e32 v156, 48, v162
	v_or_b32_e32 v38, v23, v24
	v_lshrrev_b32_e32 v23, 5, v156
	v_and_or_b32 v23, v23, s45, v21
	v_lshlrev_b32_e32 v39, 14, v23
	v_and_or_b32 v23, v156, 48, v22
	v_lshrrev_b32_e32 v23, 1, v23
	v_add_u32_e32 v154, 64, v162
	v_or_b32_e32 v40, v23, v24
	v_lshrrev_b32_e32 v23, 5, v154
	v_and_or_b32 v23, v23, s45, v21
	v_add_u32_e32 v152, 0x50, v162
	v_lshlrev_b32_e32 v41, 14, v23
	v_lshrrev_b32_e32 v23, 5, v152
	v_and_or_b32 v23, v23, s45, v21
	v_lshlrev_b32_e32 v42, 14, v23
	v_and_or_b32 v23, v152, 48, v22
	v_lshrrev_b32_e32 v23, 1, v23
	v_add_u32_e32 v150, 0x60, v162
	v_or_b32_e32 v43, v23, v24
	v_lshrrev_b32_e32 v23, 5, v150
	v_and_or_b32 v23, v23, s45, v21
	v_add_u32_e32 v148, 0x70, v162
	v_lshlrev_b32_e32 v44, 14, v23
	v_and_or_b32 v23, v150, 48, v22
	v_and_or_b32 v22, v148, 48, v22
	v_lshrrev_b32_e32 v22, 1, v22
	v_lshrrev_b32_e32 v23, 1, v23
	v_or_b32_e32 v46, v22, v24
	v_lshl_add_u32 v22, v162, 3, 0
	v_or_b32_e32 v45, v23, v24
	v_lshrrev_b32_e32 v23, 5, v148
	v_add_u32_e32 v47, 0x20400, v22
	v_and_or_b32 v21, v23, s45, v21
	ds_read_b64 v[22:23], v47
	v_lshlrev_b32_e32 v26, 16, v66
	v_and_b32_e32 v27, 0xffff0000, v66
	v_lshlrev_b32_e32 v24, 16, v67
	v_and_b32_e32 v25, 0xffff0000, v67
	v_lshlrev_b32_e32 v30, 16, v68
	v_and_b32_e32 v31, 0xffff0000, v68
	v_lshlrev_b32_e32 v28, 16, v69
	v_and_b32_e32 v29, 0xffff0000, v69
	s_waitcnt lgkmcnt(0)
	v_sub_f32_e32 v27, v27, v22
	v_sub_f32_e32 v26, v26, v22
	v_sub_f32_e32 v25, v25, v22
	v_sub_f32_e32 v24, v24, v22
	v_pk_mul_f32 v[26:27], v[22:23], v[26:27] op_sel:[1,0]
	v_sub_f32_e32 v29, v29, v22
	v_sub_f32_e32 v28, v28, v22
	v_sub_f32_e32 v31, v31, v22
	v_sub_f32_e32 v30, v30, v22
	v_pk_mul_f32 v[24:25], v[22:23], v[24:25] op_sel:[1,0]
	s_cmp_eq_u32 s100, s18
	s_cbranch_scc1 .Lsp_ln_restore
	s_waitcnt vmcnt(0)
	v_mov_b32_e32 v240, v2
	v_mov_b32_e32 v241, v3
	v_mov_b32_e32 v242, v4
	v_mov_b32_e32 v243, v5
	v_mov_b32_e32 v244, v6
	v_mov_b32_e32 v245, v7
	v_mov_b32_e32 v246, v8
	v_mov_b32_e32 v247, v9
	v_mov_b32_e32 v248, v10
	v_mov_b32_e32 v249, v11
	v_mov_b32_e32 v250, v12
	v_mov_b32_e32 v251, v13
	v_mov_b32_e32 v252, v14
	v_mov_b32_e32 v253, v15
	v_mov_b32_e32 v254, v16
	v_mov_b32_e32 v255, v17
	s_branch .Lsp_ln_ok
; __device__ __forceinline__ u32x4 pack8(f32x4 v0, f32x4 v1) { u32x4 w; w.x = cvt_pk_bf16(v0[0], v0[1]); w.y = cvt_pk_bf16(v0[2], v0[3]); w.z = cvt_pk_bf16(v1[0], v1[1]); w.w = cvt_pk_bf16(v1[2], v1[3]); return w; }
; __device__ __forceinline__ void gmlp_spatial_fused(Frame& F, int j, int row0) {
;     ...
;         { const f32x4 ga = *(const f32x4*)(lng + 256 * g + 8 * c8), gb = *(const f32x4*)(lng + 256 * g + 8 * c8 + 4), ba = *(const f32x4*)(lnb + 256 * g + 8 * c8), bb = *(const f32x4*)(lnb + 256 * g + 8 * c8 + 4);
; #pragma unroll
;           for (int i = 0; i < 8; ++i) { const f32x2 st = stl[q0 + 16 * i]; const u32x4 w = zin[i];
;               f32x4 x0 = (f32x4){bflo(w.x), bfhi(w.x), bflo(w.y), bfhi(w.y)}, x1 = (f32x4){bflo(w.z), bfhi(w.z), bflo(w.w), bfhi(w.w)};
;               x0 = (x0 - st.x) * st.y * ga + ba; x1 = (x1 - st.x) * st.y * gb + bb;
;               *(u32x4*)(lds + sto[i]) = pg8::pack8(x0, x1); } }
.Lsp_ln_restore:
	v_mov_b32_e32 v2, v240
	v_mov_b32_e32 v3, v241
	v_mov_b32_e32 v4, v242
	v_mov_b32_e32 v5, v243
	v_mov_b32_e32 v6, v244
	v_mov_b32_e32 v7, v245
	v_mov_b32_e32 v8, v246
	v_mov_b32_e32 v9, v247
	v_mov_b32_e32 v10, v248
	v_mov_b32_e32 v11, v249
	v_mov_b32_e32 v12, v250
	v_mov_b32_e32 v13, v251
	v_mov_b32_e32 v14, v252
	v_mov_b32_e32 v15, v253
	v_mov_b32_e32 v16, v254
	v_mov_b32_e32 v17, v255
.Lsp_ln_ok:
	v_pk_fma_f32 v[26:27], v[10:11], v[26:27], v[14:15]
	v_pk_mul_f32 v[30:31], v[22:23], v[30:31] op_sel:[1,0]
	v_pk_mul_f32 v[22:23], v[22:23], v[28:29] op_sel:[1,0]
	v_lshl_add_u32 v34, v34, 9, 0
	v_pk_fma_f32 v[24:25], v[12:13], v[24:25], v[16:17]
	v_pk_fma_f32 v[28:29], v[4:5], v[22:23], v[8:9]
	v_cvt_pk_bf16_f32 v22, v26, v27
	v_add3_u32 v26, v34, v33, v32
	v_pk_fma_f32 v[30:31], v[2:3], v[30:31], v[6:7]
	v_cvt_pk_bf16_f32 v23, v24, v25
	v_and_b32_e32 v27, 0xffff0000, v70
	v_cvt_pk_bf16_f32 v24, v30, v31
	v_cvt_pk_bf16_f32 v25, v28, v29
	ds_write_b128 v26, v[22:25]
	ds_read_b64 v[22:23], v47 offset:128
	v_lshlrev_b32_e32 v26, 16, v70
	v_lshlrev_b32_e32 v24, 16, v71
	v_and_b32_e32 v25, 0xffff0000, v71
	v_lshlrev_b32_e32 v30, 16, v72
	v_and_b32_e32 v31, 0xffff0000, v72
	v_lshlrev_b32_e32 v28, 16, v73
	v_and_b32_e32 v29, 0xffff0000, v73
	s_waitcnt lgkmcnt(0)
	v_sub_f32_e32 v27, v27, v22
	v_sub_f32_e32 v26, v26, v22
	v_sub_f32_e32 v25, v25, v22
	v_sub_f32_e32 v24, v24, v22
	v_pk_mul_f32 v[26:27], v[22:23], v[26:27] op_sel:[1,0]
	v_sub_f32_e32 v29, v29, v22
	v_sub_f32_e32 v28, v28, v22
	v_sub_f32_e32 v31, v31, v22
	v_sub_f32_e32 v30, v30, v22
	v_pk_mul_f32 v[24:25], v[22:23], v[24:25] op_sel:[1,0]
	v_pk_fma_f32 v[26:27], v[10:11], v[26:27], v[14:15]
	v_pk_mul_f32 v[30:31], v[22:23], v[30:31] op_sel:[1,0]
	v_pk_mul_f32 v[22:23], v[22:23], v[28:29] op_sel:[1,0]
	v_pk_fma_f32 v[24:25], v[12:13], v[24:25], v[16:17]
	v_pk_fma_f32 v[28:29], v[4:5], v[22:23], v[8:9]
	v_cvt_pk_bf16_f32 v22, v26, v27
	v_lshl_add_u32 v26, v36, 9, 0
	v_add3_u32 v26, v26, v35, v32
	v_pk_fma_f32 v[30:31], v[2:3], v[30:31], v[6:7]
	v_cvt_pk_bf16_f32 v23, v24, v25
	v_and_b32_e32 v27, 0xffff0000, v74
	v_cvt_pk_bf16_f32 v24, v30, v31
	v_cvt_pk_bf16_f32 v25, v28, v29
	ds_write_b128 v26, v[22:25]
	ds_read_b64 v[22:23], v47 offset:256
	v_lshlrev_b32_e32 v26, 16, v74
	v_lshlrev_b32_e32 v24, 16, v75
	v_and_b32_e32 v25, 0xffff0000, v75
	v_lshlrev_b32_e32 v30, 16, v76
	v_and_b32_e32 v31, 0xffff0000, v76
	v_lshlrev_b32_e32 v28, 16, v77
	v_and_b32_e32 v29, 0xffff0000, v77
	s_waitcnt lgkmcnt(0)
	v_sub_f32_e32 v27, v27, v22
	v_sub_f32_e32 v26, v26, v22
	v_sub_f32_e32 v25, v25, v22
	v_sub_f32_e32 v24, v24, v22
	v_pk_mul_f32 v[26:27], v[22:23], v[26:27] op_sel:[1,0]
	v_sub_f32_e32 v29, v29, v22
	v_sub_f32_e32 v28, v28, v22
	v_sub_f32_e32 v31, v31, v22
	v_sub_f32_e32 v30, v30, v22
	v_pk_mul_f32 v[24:25], v[22:23], v[24:25] op_sel:[1,0]
	v_pk_fma_f32 v[26:27], v[10:11], v[26:27], v[14:15]
	v_pk_mul_f32 v[30:31], v[22:23], v[30:31] op_sel:[1,0]
	v_pk_mul_f32 v[22:23], v[22:23], v[28:29] op_sel:[1,0]
	v_pk_fma_f32 v[24:25], v[12:13], v[24:25], v[16:17]
	v_pk_fma_f32 v[28:29], v[4:5], v[22:23], v[8:9]
	v_cvt_pk_bf16_f32 v22, v26, v27
	v_lshl_add_u32 v26, v38, 9, 0
	v_add3_u32 v26, v26, v37, v32
	v_pk_fma_f32 v[30:31], v[2:3], v[30:31], v[6:7]
	v_cvt_pk_bf16_f32 v23, v24, v25
	v_and_b32_e32 v27, 0xffff0000, v78
	v_cvt_pk_bf16_f32 v24, v30, v31
	v_cvt_pk_bf16_f32 v25, v28, v29
	ds_write_b128 v26, v[22:25]
	ds_read_b64 v[22:23], v47 offset:384
	v_lshlrev_b32_e32 v26, 16, v78
	v_lshlrev_b32_e32 v24, 16, v79
	v_and_b32_e32 v25, 0xffff0000, v79
	v_lshlrev_b32_e32 v30, 16, v80
	v_and_b32_e32 v31, 0xffff0000, v80
	v_lshlrev_b32_e32 v28, 16, v81
	v_and_b32_e32 v29, 0xffff0000, v81
	s_waitcnt lgkmcnt(0)
	v_sub_f32_e32 v27, v27, v22
	v_sub_f32_e32 v26, v26, v22
	v_sub_f32_e32 v25, v25, v22
	v_sub_f32_e32 v24, v24, v22
	v_pk_mul_f32 v[26:27], v[22:23], v[26:27] op_sel:[1,0]
	v_sub_f32_e32 v29, v29, v22
	v_sub_f32_e32 v28, v28, v22
	v_sub_f32_e32 v31, v31, v22
	v_sub_f32_e32 v30, v30, v22
	v_pk_mul_f32 v[24:25], v[22:23], v[24:25] op_sel:[1,0]
	v_pk_fma_f32 v[26:27], v[10:11], v[26:27], v[14:15]
	v_pk_mul_f32 v[30:31], v[22:23], v[30:31] op_sel:[1,0]
	v_pk_mul_f32 v[22:23], v[22:23], v[28:29] op_sel:[1,0]
	v_pk_fma_f32 v[24:25], v[12:13], v[24:25], v[16:17]
	v_pk_fma_f32 v[28:29], v[4:5], v[22:23], v[8:9]
	v_cvt_pk_bf16_f32 v22, v26, v27
	v_lshl_add_u32 v26, v40, 9, 0
	v_add3_u32 v26, v26, v39, v32
	v_pk_fma_f32 v[30:31], v[2:3], v[30:31], v[6:7]
	v_cvt_pk_bf16_f32 v23, v24, v25
	v_and_b32_e32 v27, 0xffff0000, v82
	v_cvt_pk_bf16_f32 v24, v30, v31
	v_cvt_pk_bf16_f32 v25, v28, v29
	ds_write_b128 v26, v[22:25]
	ds_read_b64 v[22:23], v47 offset:512
	v_lshlrev_b32_e32 v26, 16, v82
	v_lshlrev_b32_e32 v24, 16, v83
	v_and_b32_e32 v25, 0xffff0000, v83
	v_lshlrev_b32_e32 v30, 16, v84
	v_and_b32_e32 v31, 0xffff0000, v84
	v_lshlrev_b32_e32 v28, 16, v85
	v_and_b32_e32 v29, 0xffff0000, v85
	s_waitcnt lgkmcnt(0)
	v_sub_f32_e32 v27, v27, v22
	v_sub_f32_e32 v26, v26, v22
	v_sub_f32_e32 v25, v25, v22
	v_sub_f32_e32 v24, v24, v22
	v_pk_mul_f32 v[26:27], v[22:23], v[26:27] op_sel:[1,0]
	v_sub_f32_e32 v29, v29, v22
	v_sub_f32_e32 v28, v28, v22
	v_sub_f32_e32 v31, v31, v22
	v_sub_f32_e32 v30, v30, v22
	v_pk_mul_f32 v[24:25], v[22:23], v[24:25] op_sel:[1,0]
	v_pk_fma_f32 v[26:27], v[10:11], v[26:27], v[14:15]
	v_pk_mul_f32 v[30:31], v[22:23], v[30:31] op_sel:[1,0]
	v_pk_mul_f32 v[22:23], v[22:23], v[28:29] op_sel:[1,0]
	v_pk_fma_f32 v[24:25], v[12:13], v[24:25], v[16:17]
	v_pk_fma_f32 v[28:29], v[4:5], v[22:23], v[8:9]
	v_cvt_pk_bf16_f32 v22, v26, v27
	v_add3_u32 v26, v34, v41, v32
	v_pk_fma_f32 v[30:31], v[2:3], v[30:31], v[6:7]
	v_cvt_pk_bf16_f32 v23, v24, v25
	v_and_b32_e32 v27, 0xffff0000, v86
	v_cvt_pk_bf16_f32 v24, v30, v31
	v_cvt_pk_bf16_f32 v25, v28, v29
	ds_write_b128 v26, v[22:25]
	ds_read_b64 v[22:23], v47 offset:640
	v_lshlrev_b32_e32 v26, 16, v86
	v_lshlrev_b32_e32 v24, 16, v87
	v_and_b32_e32 v25, 0xffff0000, v87
	v_lshlrev_b32_e32 v30, 16, v88
	v_and_b32_e32 v31, 0xffff0000, v88
	v_lshlrev_b32_e32 v28, 16, v89
	v_and_b32_e32 v29, 0xffff0000, v89
	s_waitcnt lgkmcnt(0)
; __device__ __forceinline__ u32x4 pack8(f32x4 v0, f32x4 v1) { u32x4 w; w.x = cvt_pk_bf16(v0[0], v0[1]); w.y = cvt_pk_bf16(v0[2], v0[3]); w.z = cvt_pk_bf16(v1[0], v1[1]); w.w = cvt_pk_bf16(v1[2], v1[3]); return w; }
; #define SP_LOAD(uu) do { const int ch_ = ch0 + ((uu) >> 3), g_ = (uu) & 7; _Pragma("unroll") for (int i = 0; i < 8; ++i) zin[i] = *(const u32x4*)(Z + (size_t)(ch_ * 128 + q0 + 16 * i) * 4096 + 2048 + 256 * g_ + 8 * c8); \
;         _Pragma("unroll") for (int i = 0; i < 4; ++i) pin[i] = *(const f32x4*)(PART + ((size_t)(ch_ * 128 + (tid >> 2)) * 32 + 8 * (tid & 3)) * 2 + 4 * i); } while (0)
; __device__ __forceinline__ void gmlp_spatial_fused(Frame& F, int j, int row0) {
;     ...
;         { const f32x4 ga = *(const f32x4*)(lng + 256 * g + 8 * c8), gb = *(const f32x4*)(lng + 256 * g + 8 * c8 + 4), ba = *(const f32x4*)(lnb + 256 * g + 8 * c8), bb = *(const f32x4*)(lnb + 256 * g + 8 * c8 + 4);
; #pragma unroll
;           for (int i = 0; i < 8; ++i) { const f32x2 st = stl[q0 + 16 * i]; const u32x4 w = zin[i];
;               f32x4 x0 = (f32x4){bflo(w.x), bfhi(w.x), bflo(w.y), bfhi(w.y)}, x1 = (f32x4){bflo(w.z), bfhi(w.z), bflo(w.w), bfhi(w.w)};
;               x0 = (x0 - st.x) * st.y * ga + ba; x1 = (x1 - st.x) * st.y * gb + bb;
;               *(u32x4*)(lds + sto[i]) = pg8::pack8(x0, x1); } }
;         asm volatile("s_waitcnt vmcnt(0) lgkmcnt(0)" ::: "memory");
;         __syncthreads();
;         const int un = u + F.G;
;         u32x4 uin[8];
; #pragma unroll
;         for (int i = 0; i < 8; ++i) uin[i] = *(const u32x4*)(Z + ((size_t)chunk * 128 + q0 + 16 * i) * 4096 + 256 * g + 8 * c8);
;         if (un < nunit) SP_LOAD(un);
	v_sub_f32_e32 v27, v27, v22
	v_sub_f32_e32 v26, v26, v22
	v_sub_f32_e32 v25, v25, v22
	v_sub_f32_e32 v24, v24, v22
	v_pk_mul_f32 v[26:27], v[22:23], v[26:27] op_sel:[1,0]
	v_sub_f32_e32 v29, v29, v22
	v_sub_f32_e32 v28, v28, v22
	v_sub_f32_e32 v31, v31, v22
	v_sub_f32_e32 v30, v30, v22
	v_pk_mul_f32 v[24:25], v[22:23], v[24:25] op_sel:[1,0]
	v_pk_fma_f32 v[26:27], v[10:11], v[26:27], v[14:15]
	v_pk_mul_f32 v[30:31], v[22:23], v[30:31] op_sel:[1,0]
	v_pk_mul_f32 v[22:23], v[22:23], v[28:29] op_sel:[1,0]
	v_pk_fma_f32 v[24:25], v[12:13], v[24:25], v[16:17]
	v_pk_fma_f32 v[28:29], v[4:5], v[22:23], v[8:9]
	v_cvt_pk_bf16_f32 v22, v26, v27
	v_lshl_add_u32 v26, v43, 9, 0
	v_add3_u32 v26, v26, v42, v32
	v_pk_fma_f32 v[30:31], v[2:3], v[30:31], v[6:7]
	v_cvt_pk_bf16_f32 v23, v24, v25
	v_and_b32_e32 v27, 0xffff0000, v90
	v_cvt_pk_bf16_f32 v24, v30, v31
	v_cvt_pk_bf16_f32 v25, v28, v29
	ds_write_b128 v26, v[22:25]
	ds_read_b64 v[22:23], v47 offset:768
	v_lshlrev_b32_e32 v26, 16, v90
	v_lshlrev_b32_e32 v24, 16, v91
	v_and_b32_e32 v25, 0xffff0000, v91
	v_lshlrev_b32_e32 v30, 16, v92
	v_and_b32_e32 v31, 0xffff0000, v92
	v_lshlrev_b32_e32 v28, 16, v93
	v_and_b32_e32 v29, 0xffff0000, v93
	s_waitcnt lgkmcnt(0)
	v_sub_f32_e32 v27, v27, v22
	v_sub_f32_e32 v26, v26, v22
	v_sub_f32_e32 v25, v25, v22
	v_sub_f32_e32 v24, v24, v22
	v_pk_mul_f32 v[26:27], v[22:23], v[26:27] op_sel:[1,0]
	v_sub_f32_e32 v29, v29, v22
	v_sub_f32_e32 v28, v28, v22
	v_sub_f32_e32 v31, v31, v22
	v_sub_f32_e32 v30, v30, v22
	v_pk_mul_f32 v[24:25], v[22:23], v[24:25] op_sel:[1,0]
	v_pk_fma_f32 v[26:27], v[10:11], v[26:27], v[14:15]
	v_pk_mul_f32 v[30:31], v[22:23], v[30:31] op_sel:[1,0]
	v_pk_mul_f32 v[22:23], v[22:23], v[28:29] op_sel:[1,0]
	v_pk_fma_f32 v[24:25], v[12:13], v[24:25], v[16:17]
	v_pk_fma_f32 v[28:29], v[4:5], v[22:23], v[8:9]
	v_cvt_pk_bf16_f32 v22, v26, v27
	v_lshl_add_u32 v26, v45, 9, 0
	v_add3_u32 v26, v26, v44, v32
	v_pk_fma_f32 v[30:31], v[2:3], v[30:31], v[6:7]
	v_cvt_pk_bf16_f32 v23, v24, v25
	v_and_b32_e32 v27, 0xffff0000, v94
	v_cvt_pk_bf16_f32 v24, v30, v31
	v_cvt_pk_bf16_f32 v25, v28, v29
	ds_write_b128 v26, v[22:25]
	ds_read_b64 v[22:23], v47 offset:896
	v_lshlrev_b32_e32 v26, 16, v94
	v_lshlrev_b32_e32 v24, 16, v95
	v_and_b32_e32 v25, 0xffff0000, v95
	v_lshlrev_b32_e32 v28, 16, v96
	s_waitcnt lgkmcnt(0)
	v_sub_f32_e32 v25, v25, v22
	v_sub_f32_e32 v24, v24, v22
	v_sub_f32_e32 v27, v27, v22
	v_sub_f32_e32 v26, v26, v22
	v_and_b32_e32 v29, 0xffff0000, v96
	v_lshlrev_b32_e32 v30, 16, v97
	v_and_b32_e32 v31, 0xffff0000, v97
	v_pk_mul_f32 v[26:27], v[22:23], v[26:27] op_sel:[1,0]
	v_pk_mul_f32 v[24:25], v[22:23], v[24:25] op_sel:[1,0]
	v_pk_fma_f32 v[10:11], v[10:11], v[26:27], v[14:15]
	v_pk_fma_f32 v[12:13], v[12:13], v[24:25], v[16:17]
	v_sub_f32_e32 v15, v31, v22
	v_sub_f32_e32 v14, v30, v22
	v_sub_f32_e32 v17, v29, v22
	v_sub_f32_e32 v16, v28, v22
	v_pk_mul_f32 v[16:17], v[22:23], v[16:17] op_sel:[1,0]
	v_pk_mul_f32 v[14:15], v[22:23], v[14:15] op_sel:[1,0]
	s_ashr_i32 s77, s76, 31
	s_lshl_b32 s1, s18, 9
	v_lshlrev_b32_e32 v21, 14, v21
	v_pk_fma_f32 v[8:9], v[4:5], v[14:15], v[8:9]
	v_pk_fma_f32 v[4:5], v[2:3], v[16:17], v[6:7]
	v_lshl_add_u32 v6, v46, 9, 0
	s_add_u32 s2, s4, s1
	v_cvt_pk_bf16_f32 v2, v10, v11
	v_cvt_pk_bf16_f32 v3, v12, v13
	v_add3_u32 v6, v6, v21, v32
	s_addc_u32 s3, s5, 0
	v_cvt_pk_bf16_f32 v4, v4, v5
	v_cvt_pk_bf16_f32 v5, v8, v9
	ds_write_b128 v6, v[2:5]
	v_ashrrev_i32_e32 v163, 31, v162
	v_lshl_add_u64 v[2:3], s[2:3], 0, v[0:1]
	s_lshl_b64 s[2:3], s[76:77], 20
	v_lshlrev_b64 v[4:5], 13, v[162:163]
	v_lshl_add_u64 v[2:3], v[2:3], 0, s[2:3]
	v_lshl_add_u64 v[2:3], v[2:3], 0, v[4:5]
	s_mov_b32 s1, 0x20000
	v_add_co_u32_e32 v4, vcc, s1, v2
	s_cmp_eq_u32 s100, s18
	s_cbranch_scc1 .Lsp_w5_skip
	s_waitcnt vmcnt(0)
.Lsp_w5_skip:
	s_waitcnt lgkmcnt(0)
	s_mov_b32 s100, s18
	s_waitcnt lgkmcnt(0)
	s_nop 0
	v_addc_co_u32_e32 v5, vcc, 0, v3, vcc
	s_barrier
	global_load_dwordx4 v[142:145], v[2:3], off
	global_load_dwordx4 v[138:141], v[4:5], off
	v_add_co_u32_e32 v4, vcc, s47, v2
	s_mov_b32 s1, 0x60000
	s_nop 0
	v_addc_co_u32_e32 v5, vcc, 0, v3, vcc
	v_add_co_u32_e32 v6, vcc, s1, v2
	s_mov_b32 s1, 0x80000
	s_nop 0
	v_addc_co_u32_e32 v7, vcc, 0, v3, vcc
	global_load_dwordx4 v[134:137], v[4:5], off
	global_load_dwordx4 v[130:133], v[6:7], off
	v_add_co_u32_e32 v4, vcc, s1, v2
	s_mov_b32 s1, 0xa0000
	s_nop 0
	v_addc_co_u32_e32 v5, vcc, 0, v3, vcc
	v_add_co_u32_e32 v6, vcc, s1, v2
	s_add_i32 s10, s10, s11
	s_nop 0
	v_addc_co_u32_e32 v7, vcc, 0, v3, vcc
	global_load_dwordx4 v[126:129], v[4:5], off
	global_load_dwordx4 v[122:125], v[6:7], off
	v_add_co_u32_e32 v4, vcc, 0xc0000, v2
	s_cmp_ge_i32 s10, s74
	s_nop 0
	v_addc_co_u32_e32 v5, vcc, 0, v3, vcc
	v_add_co_u32_e32 v2, vcc, 0xe0000, v2
	v_lshlrev_b32_e32 v0, 3, v147
	s_nop 0
	v_addc_co_u32_e32 v3, vcc, 0, v3, vcc
	global_load_dwordx4 v[118:121], v[4:5], off
	global_load_dwordx4 v[114:117], v[2:3], off
	s_cselect_b64 s[2:3], -1, 0
	s_and_b64 vcc, exec, s[2:3]
	v_lshlrev_b32_e32 v0, 1, v0
	s_cbranch_vccnz .LBB0_582
	s_lshr_b32 s1, s10, 3
	s_add_i32 s1, s1, s25
	s_lshl_b32 s1, s1, 7
	v_add_u32_e32 v2, s1, v162
	v_ashrrev_i32_e32 v3, 31, v2
	s_and_b32 s12, s51, 0x700
	v_lshlrev_b64 v[2:3], 13, v[2:3]
	v_lshl_add_u64 v[2:3], s[4:5], 0, v[2:3]
	s_lshl_b32 s18, s12, 1
	v_lshl_add_u64 v[2:3], v[2:3], 0, s[18:19]
	v_lshl_add_u64 v[2:3], v[2:3], 0, v[0:1]
	v_add_co_u32_e32 v4, vcc, s58, v2
	s_nop 1
	v_addc_co_u32_e32 v5, vcc, 0, v3, vcc
	v_add_co_u32_e32 v6, vcc, s59, v2
	s_nop 1
	v_addc_co_u32_e32 v7, vcc, 0, v3, vcc
	global_load_dwordx4 v[66:69], v[4:5], off
	global_load_dwordx4 v[70:73], v[6:7], off
	v_add_co_u32_e32 v4, vcc, s60, v2
	s_nop 1
	v_addc_co_u32_e32 v5, vcc, 0, v3, vcc
	v_add_co_u32_e32 v6, vcc, s61, v2
	s_nop 1
	v_addc_co_u32_e32 v7, vcc, 0, v3, vcc
	global_load_dwordx4 v[74:77], v[4:5], off
	global_load_dwordx4 v[78:81], v[6:7], off
	v_add_co_u32_e32 v4, vcc, s64, v2
	s_nop 1
	v_addc_co_u32_e32 v5, vcc, 0, v3, vcc
	v_add_co_u32_e32 v6, vcc, s65, v2
	s_nop 1
	v_addc_co_u32_e32 v7, vcc, 0, v3, vcc
	global_load_dwordx4 v[82:85], v[4:5], off
	global_load_dwordx4 v[86:89], v[6:7], off
	v_add_co_u32_e32 v4, vcc, s66, v2
	s_nop 1
	v_addc_co_u32_e32 v5, vcc, 0, v3, vcc
	v_add_co_u32_e32 v2, vcc, s67, v2
	s_nop 1
	v_addc_co_u32_e32 v3, vcc, 0, v3, vcc
	global_load_dwordx4 v[90:93], v[4:5], off
	global_load_dwordx4 v[94:97], v[2:3], off
	v_ashrrev_i32_e32 v2, 2, v19
	v_add_u32_e32 v2, s1, v2
	v_ashrrev_i32_e32 v3, 31, v2
	v_lshlrev_b64 v[2:3], 8, v[2:3]
	v_lshl_add_u64 v[2:3], s[6:7], 0, v[2:3]
	v_lshlrev_b32_e32 v4, 6, v20
	v_mov_b32_e32 v5, v1
	v_lshl_add_u64 v[2:3], v[2:3], 0, v[4:5]
	global_load_dwordx4 v[98:101], v[2:3], off offset:48
	global_load_dwordx4 v[102:105], v[2:3], off offset:32
	global_load_dwordx4 v[106:109], v[2:3], off offset:16
	global_load_dwordx4 v[110:113], v[2:3], off
	s_branch .LBB0_582
